# router: the 8 expert counters moved to separate cache lines (stride 0x2100 B) so the 32768 slot atomics no longer serialize on one line
# speedup vs baseline: 1.0651x; 1.0651x over previous
.LBB0_1622:
	v_lshl_add_u64 v[0:1], s[52:53], 0, v[18:19]
	s_waitcnt lgkmcnt(0)
	v_add_co_u32_e32 v20, vcc, 0x2d000000, v0
	s_nop 1
	v_addc_co_u32_e32 v21, vcc, 0, v1, vcc
	global_load_dwordx2 v[0:1], v[20:21], off
	s_waitcnt vmcnt(0)
	v_lshlrev_b32_e32 v26, 16, v0
	v_and_b32_e32 v28, 0xffff0000, v0
	v_lshlrev_b32_e32 v30, 16, v1
	v_and_b32_e32 v32, 0xffff0000, v1
	ds_read_b128 v[0:3], v25
	ds_read_b128 v[4:7], v25 offset:32768
	v_mul_f32_e32 v40, v28, v28
	v_fmac_f32_e32 v40, v26, v26
	v_fmac_f32_e32 v40, v30, v30
	s_waitcnt lgkmcnt(1)
	v_fma_f32 v39, v2, v26, 0
	v_fma_f32 v37, v3, v26, 0
	s_waitcnt lgkmcnt(0)
	v_fma_f32 v35, v4, v26, 0
	v_fma_f32 v33, v5, v26, 0
	v_fma_f32 v31, v6, v26, 0
	v_fma_f32 v29, v7, v26, 0
	ds_read_b128 v[2:5], v25 offset:8192
	ds_read_b128 v[6:9], v25 offset:40960
	v_pk_fma_f32 v[0:1], v[0:1], v[26:27], 0 op_sel_hi:[1,0,0]
	v_fmac_f32_e32 v40, v32, v32
	s_waitcnt lgkmcnt(1)
	v_fmac_f32_e32 v39, v4, v28
	v_fmac_f32_e32 v37, v5, v28
	s_waitcnt lgkmcnt(0)
	v_fmac_f32_e32 v35, v6, v28
	v_fmac_f32_e32 v33, v7, v28
	v_fmac_f32_e32 v31, v8, v28
	v_fmac_f32_e32 v29, v9, v28
	ds_read_b128 v[4:7], v25 offset:16384
	ds_read_b128 v[8:11], v25 offset:49152
	s_waitcnt lgkmcnt(1)
	v_fmac_f32_e32 v39, v6, v30
	v_fmac_f32_e32 v37, v7, v30
	s_waitcnt lgkmcnt(0)
	v_fmac_f32_e32 v35, v8, v30
	v_fmac_f32_e32 v33, v9, v30
	v_fmac_f32_e32 v31, v10, v30
	v_fmac_f32_e32 v29, v11, v30
	ds_read_b128 v[6:9], v25 offset:24576
	ds_read_b128 v[10:13], v25 offset:57344
	s_waitcnt lgkmcnt(1)
	v_fmac_f32_e32 v39, v8, v32
	v_fmac_f32_e32 v37, v9, v32
	global_load_dwordx2 v[8:9], v[20:21], off offset:512
	s_waitcnt lgkmcnt(0)
	v_fmac_f32_e32 v35, v10, v32
	v_fmac_f32_e32 v33, v11, v32
	v_fmac_f32_e32 v31, v12, v32
	v_fmac_f32_e32 v29, v13, v32
	v_pk_fma_f32 v[0:1], v[2:3], v[28:29], v[0:1] op_sel_hi:[1,0,1]
	s_waitcnt vmcnt(0)
	v_lshlrev_b32_e32 v34, 16, v8
	v_and_b32_e32 v16, 0xffff0000, v8
	v_lshlrev_b32_e32 v22, 16, v9
	v_and_b32_e32 v24, 0xffff0000, v9
	ds_read_b128 v[8:11], v25 offset:1024
	ds_read_b128 v[12:15], v25 offset:33792
	v_pk_fma_f32 v[0:1], v[4:5], v[30:31], v[0:1] op_sel_hi:[1,0,1]
	v_fmac_f32_e32 v40, v34, v34
	v_pk_fma_f32 v[0:1], v[6:7], v[32:33], v[0:1] op_sel_hi:[1,0,1]
	s_waitcnt lgkmcnt(1)
	v_fmac_f32_e32 v39, v10, v34
	v_pk_fma_f32 v[26:27], v[8:9], v[34:35], v[0:1] op_sel_hi:[1,0,1]
	ds_read_b128 v[0:3], v25 offset:9216
	ds_read_b128 v[4:7], v25 offset:41984
	v_fmac_f32_e32 v37, v11, v34
	s_waitcnt lgkmcnt(2)
	v_fmac_f32_e32 v35, v12, v34
	v_fmac_f32_e32 v33, v13, v34
	v_fmac_f32_e32 v31, v14, v34
	v_fmac_f32_e32 v29, v15, v34
	s_waitcnt lgkmcnt(1)
	v_fmac_f32_e32 v39, v2, v16
	v_fmac_f32_e32 v37, v3, v16
	s_waitcnt lgkmcnt(0)
	v_fmac_f32_e32 v35, v4, v16
	v_fmac_f32_e32 v33, v5, v16
	v_fmac_f32_e32 v31, v6, v16
	v_fmac_f32_e32 v29, v7, v16
	ds_read_b128 v[2:5], v25 offset:17408
	ds_read_b128 v[6:9], v25 offset:50176
	v_pk_fma_f32 v[0:1], v[0:1], v[16:17], v[26:27] op_sel_hi:[1,0,1]
	v_fmac_f32_e32 v40, v16, v16
	v_fmac_f32_e32 v40, v22, v22
	s_waitcnt lgkmcnt(1)
	v_fmac_f32_e32 v39, v4, v22
	v_fmac_f32_e32 v37, v5, v22
	s_waitcnt lgkmcnt(0)
	v_fmac_f32_e32 v35, v6, v22
	v_fmac_f32_e32 v33, v7, v22
	v_fmac_f32_e32 v31, v8, v22
	v_fmac_f32_e32 v29, v9, v22
	ds_read_b128 v[4:7], v25 offset:25600
	ds_read_b128 v[8:11], v25 offset:58368
	v_pk_fma_f32 v[0:1], v[2:3], v[22:23], v[0:1] op_sel_hi:[1,0,1]
	v_fmac_f32_e32 v40, v24, v24
	s_waitcnt lgkmcnt(1)
	v_fmac_f32_e32 v39, v6, v24
	v_fmac_f32_e32 v37, v7, v24
	global_load_dwordx2 v[6:7], v[20:21], off offset:1024
	s_waitcnt lgkmcnt(0)
	v_fmac_f32_e32 v35, v8, v24
	v_fmac_f32_e32 v33, v9, v24
	v_fmac_f32_e32 v31, v10, v24
	v_fmac_f32_e32 v29, v11, v24
	v_pk_fma_f32 v[0:1], v[4:5], v[24:25], v[0:1] op_sel_hi:[1,0,1]
	s_waitcnt vmcnt(0)
	v_lshlrev_b32_e32 v28, 16, v6
	v_and_b32_e32 v30, 0xffff0000, v6
	v_lshlrev_b32_e32 v32, 16, v7
	v_and_b32_e32 v34, 0xffff0000, v7
	ds_read_b128 v[6:9], v25 offset:2048
	ds_read_b128 v[10:13], v25 offset:34816
	v_fmac_f32_e32 v40, v28, v28
	v_fmac_f32_e32 v40, v30, v30
	v_fmac_f32_e32 v40, v32, v32
	s_waitcnt lgkmcnt(1)
	v_fmac_f32_e32 v39, v8, v28
	v_fmac_f32_e32 v37, v9, v28
	s_waitcnt lgkmcnt(0)
	v_fmac_f32_e32 v35, v10, v28
	v_fmac_f32_e32 v33, v11, v28
	v_fmac_f32_e32 v31, v12, v28
	v_fmac_f32_e32 v29, v13, v28
	ds_read_b128 v[8:11], v25 offset:10240
	ds_read_b128 v[12:15], v25 offset:43008
	v_fmac_f32_e32 v40, v34, v34
	s_waitcnt lgkmcnt(1)
	v_fmac_f32_e32 v39, v10, v30
	v_fmac_f32_e32 v37, v11, v30
	s_waitcnt lgkmcnt(0)
	v_fmac_f32_e32 v35, v12, v30
	v_fmac_f32_e32 v33, v13, v30
	ds_read_b128 v[10:13], v25 offset:18432
	ds_read_b128 v[42:45], v25 offset:51200
	v_fmac_f32_e32 v31, v14, v30
	v_fmac_f32_e32 v29, v15, v30
	s_waitcnt lgkmcnt(1)
	v_fmac_f32_e32 v39, v12, v32
	v_fmac_f32_e32 v37, v13, v32
	s_waitcnt lgkmcnt(0)
	v_fmac_f32_e32 v35, v42, v32
	v_fmac_f32_e32 v33, v43, v32
	v_fmac_f32_e32 v31, v44, v32
	v_fmac_f32_e32 v29, v45, v32
	ds_read_b128 v[12:15], v25 offset:26624
	ds_read_b128 v[42:45], v25 offset:59392
	s_waitcnt lgkmcnt(1)
	v_fmac_f32_e32 v39, v14, v34
	v_fmac_f32_e32 v37, v15, v34
	global_load_dwordx2 v[14:15], v[20:21], off offset:1536
	s_waitcnt lgkmcnt(0)
	v_fmac_f32_e32 v35, v42, v34
	v_fmac_f32_e32 v33, v43, v34
	v_fmac_f32_e32 v31, v44, v34
	v_fmac_f32_e32 v29, v45, v34
	ds_read_b128 v[42:45], v25 offset:3072
	ds_read_b128 v[46:49], v25 offset:35840
	s_waitcnt vmcnt(0)
	v_lshlrev_b32_e32 v36, 16, v14
	s_waitcnt lgkmcnt(1)
	v_fmac_f32_e32 v39, v44, v36
	v_fmac_f32_e32 v37, v45, v36
	s_waitcnt lgkmcnt(0)
	v_fmac_f32_e32 v35, v46, v36
	v_fmac_f32_e32 v33, v47, v36
	v_fmac_f32_e32 v31, v48, v36
	v_fmac_f32_e32 v29, v49, v36
	ds_read_b128 v[44:47], v25 offset:11264
	ds_read_b128 v[48:51], v25 offset:44032
	v_and_b32_e32 v14, 0xffff0000, v14
	v_lshlrev_b32_e32 v38, 16, v15
	v_and_b32_e32 v56, 0xffff0000, v15
	s_waitcnt lgkmcnt(1)
	v_fmac_f32_e32 v39, v46, v14
	v_fmac_f32_e32 v37, v47, v14
	s_waitcnt lgkmcnt(0)
	v_fmac_f32_e32 v35, v48, v14
	v_fmac_f32_e32 v33, v49, v14
	v_fmac_f32_e32 v31, v50, v14
	v_fmac_f32_e32 v29, v51, v14
	ds_read_b128 v[46:49], v25 offset:19456
	ds_read_b128 v[50:53], v25 offset:52224
	v_fmac_f32_e32 v40, v36, v36
	v_fmac_f32_e32 v40, v14, v14
	v_fmac_f32_e32 v40, v38, v38
	s_waitcnt lgkmcnt(1)
	v_fmac_f32_e32 v39, v48, v38
	s_waitcnt lgkmcnt(0)
	v_fmac_f32_e32 v29, v53, v38
	v_fmac_f32_e32 v31, v52, v38
	v_pk_fma_f32 v[0:1], v[6:7], v[28:29], v[0:1] op_sel_hi:[1,0,1]
	v_fmac_f32_e32 v33, v51, v38
	v_pk_fma_f32 v[0:1], v[8:9], v[30:31], v[0:1] op_sel_hi:[1,0,1]
	v_fmac_f32_e32 v35, v50, v38
	v_pk_fma_f32 v[0:1], v[10:11], v[32:33], v[0:1] op_sel_hi:[1,0,1]
	v_fmac_f32_e32 v37, v49, v38
	ds_read_b128 v[48:51], v25 offset:27648
	ds_read_b128 v[52:55], v25 offset:60416
	v_pk_fma_f32 v[0:1], v[12:13], v[34:35], v[0:1] op_sel_hi:[1,0,1]
	v_fmac_f32_e32 v40, v56, v56
	v_pk_fma_f32 v[0:1], v[42:43], v[36:37], v[0:1] op_sel_hi:[1,0,1]
	s_waitcnt lgkmcnt(1)
	v_fmac_f32_e32 v37, v51, v56
	v_pk_fma_f32 v[0:1], v[44:45], v[14:15], v[0:1] op_sel_hi:[1,0,1]
	s_waitcnt lgkmcnt(0)
	v_fmac_f32_e32 v35, v52, v56
	v_pk_fma_f32 v[0:1], v[46:47], v[38:39], v[0:1] op_sel_hi:[1,0,1]
	v_fmac_f32_e32 v39, v50, v56
	v_pk_fma_f32 v[22:23], v[48:49], v[56:57], v[0:1] op_sel_hi:[1,0,1]
	global_load_dwordx2 v[0:1], v[20:21], off offset:2048
	v_fmac_f32_e32 v33, v53, v56
	v_fmac_f32_e32 v31, v54, v56
	v_fmac_f32_e32 v29, v55, v56
	s_waitcnt vmcnt(0)
	v_lshlrev_b32_e32 v24, 16, v0
	v_and_b32_e32 v26, 0xffff0000, v0
	v_lshlrev_b32_e32 v28, 16, v1
	v_and_b32_e32 v30, 0xffff0000, v1
	ds_read_b128 v[0:3], v25 offset:4096
	ds_read_b128 v[4:7], v25 offset:36864
	v_fmac_f32_e32 v40, v24, v24
	v_fmac_f32_e32 v40, v26, v26
	v_fmac_f32_e32 v40, v28, v28
	s_waitcnt lgkmcnt(1)
	v_fmac_f32_e32 v39, v2, v24
	v_fmac_f32_e32 v37, v3, v24
	s_waitcnt lgkmcnt(0)
	v_fmac_f32_e32 v35, v4, v24
	v_fmac_f32_e32 v33, v5, v24
	v_fmac_f32_e32 v31, v6, v24
	v_fmac_f32_e32 v29, v7, v24
	ds_read_b128 v[2:5], v25 offset:12288
	ds_read_b128 v[6:9], v25 offset:45056
	v_pk_fma_f32 v[0:1], v[0:1], v[24:25], v[22:23] op_sel_hi:[1,0,1]
	v_fmac_f32_e32 v40, v30, v30
	s_waitcnt lgkmcnt(1)
	v_fmac_f32_e32 v39, v4, v26
	v_fmac_f32_e32 v37, v5, v26
	s_waitcnt lgkmcnt(0)
	v_fmac_f32_e32 v35, v6, v26
	v_fmac_f32_e32 v33, v7, v26
	v_fmac_f32_e32 v31, v8, v26
	v_fmac_f32_e32 v29, v9, v26
	ds_read_b128 v[4:7], v25 offset:20480
	ds_read_b128 v[8:11], v25 offset:53248
	v_pk_fma_f32 v[0:1], v[2:3], v[26:27], v[0:1] op_sel_hi:[1,0,1]
	s_waitcnt lgkmcnt(1)
	v_fmac_f32_e32 v39, v6, v28
	v_fmac_f32_e32 v37, v7, v28
	s_waitcnt lgkmcnt(0)
	v_fmac_f32_e32 v35, v8, v28
	v_fmac_f32_e32 v33, v9, v28
	v_fmac_f32_e32 v31, v10, v28
	v_fmac_f32_e32 v29, v11, v28
	ds_read_b128 v[6:9], v25 offset:28672
	ds_read_b128 v[10:13], v25 offset:61440
	s_waitcnt lgkmcnt(1)
	v_fmac_f32_e32 v39, v8, v30
	v_fmac_f32_e32 v37, v9, v30
	global_load_dwordx2 v[8:9], v[20:21], off offset:2560
	s_waitcnt lgkmcnt(0)
	v_fmac_f32_e32 v35, v10, v30
	v_fmac_f32_e32 v33, v11, v30
	v_fmac_f32_e32 v31, v12, v30
	v_fmac_f32_e32 v29, v13, v30
	s_waitcnt vmcnt(0)
	v_lshlrev_b32_e32 v32, 16, v8
	v_and_b32_e32 v34, 0xffff0000, v8
	v_lshlrev_b32_e32 v36, 16, v9
	v_and_b32_e32 v38, 0xffff0000, v9
	ds_read_b128 v[8:11], v25 offset:5120
	ds_read_b128 v[12:15], v25 offset:37888
	v_fmac_f32_e32 v40, v32, v32
	v_fmac_f32_e32 v40, v34, v34
	v_fmac_f32_e32 v40, v36, v36
	s_waitcnt lgkmcnt(1)
	v_fmac_f32_e32 v39, v10, v32
	v_fmac_f32_e32 v37, v11, v32
	s_waitcnt lgkmcnt(0)
	v_fmac_f32_e32 v35, v12, v32
	v_fmac_f32_e32 v33, v13, v32
	v_fmac_f32_e32 v31, v14, v32
	v_fmac_f32_e32 v29, v15, v32
	ds_read_b128 v[10:13], v25 offset:13312
	ds_read_b128 v[14:17], v25 offset:46080
	v_fmac_f32_e32 v40, v38, v38
	s_waitcnt lgkmcnt(1)
	v_fmac_f32_e32 v39, v12, v34
	v_fmac_f32_e32 v37, v13, v34
	s_waitcnt lgkmcnt(0)
	v_fmac_f32_e32 v35, v14, v34
	v_fmac_f32_e32 v33, v15, v34
	ds_read_b128 v[12:15], v25 offset:21504
	ds_read_b128 v[42:45], v25 offset:54272
	v_fmac_f32_e32 v31, v16, v34
	v_fmac_f32_e32 v29, v17, v34
	s_waitcnt lgkmcnt(1)
	v_fmac_f32_e32 v39, v14, v36
	v_fmac_f32_e32 v37, v15, v36
	s_waitcnt lgkmcnt(0)
	v_fmac_f32_e32 v35, v42, v36
	v_fmac_f32_e32 v33, v43, v36
	v_fmac_f32_e32 v31, v44, v36
	v_fmac_f32_e32 v29, v45, v36
	ds_read_b128 v[14:17], v25 offset:29696
	ds_read_b128 v[42:45], v25 offset:62464
	s_waitcnt lgkmcnt(1)
	v_fmac_f32_e32 v39, v16, v38
	v_fmac_f32_e32 v37, v17, v38
	global_load_dwordx2 v[16:17], v[20:21], off offset:3072
	s_waitcnt lgkmcnt(0)
	v_fmac_f32_e32 v35, v42, v38
	v_fmac_f32_e32 v33, v43, v38
	v_fmac_f32_e32 v31, v44, v38
	v_fmac_f32_e32 v29, v45, v38
	ds_read_b128 v[42:45], v25 offset:6144
	ds_read_b128 v[46:49], v25 offset:38912
	s_waitcnt vmcnt(0)
	v_lshlrev_b32_e32 v54, 16, v16
	s_waitcnt lgkmcnt(1)
	v_fmac_f32_e32 v39, v44, v54
	v_fmac_f32_e32 v37, v45, v54
	s_waitcnt lgkmcnt(0)
	v_fmac_f32_e32 v35, v46, v54
	v_fmac_f32_e32 v33, v47, v54
	v_fmac_f32_e32 v31, v48, v54
	v_fmac_f32_e32 v29, v49, v54
	ds_read_b128 v[44:47], v25 offset:14336
	ds_read_b128 v[48:51], v25 offset:47104
	v_and_b32_e32 v56, 0xffff0000, v16
	v_lshlrev_b32_e32 v58, 16, v17
	v_and_b32_e32 v16, 0xffff0000, v17
	s_waitcnt lgkmcnt(1)
	v_fmac_f32_e32 v37, v47, v56
	s_waitcnt lgkmcnt(0)
	v_fmac_f32_e32 v29, v51, v56
	v_fmac_f32_e32 v31, v50, v56
	v_pk_fma_f32 v[0:1], v[4:5], v[28:29], v[0:1] op_sel_hi:[1,0,1]
	v_fmac_f32_e32 v33, v49, v56
	v_pk_fma_f32 v[0:1], v[6:7], v[30:31], v[0:1] op_sel_hi:[1,0,1]
	v_fmac_f32_e32 v35, v48, v56
	v_pk_fma_f32 v[0:1], v[8:9], v[32:33], v[0:1] op_sel_hi:[1,0,1]
	v_fmac_f32_e32 v39, v46, v56
	v_pk_fma_f32 v[0:1], v[10:11], v[34:35], v[0:1] op_sel_hi:[1,0,1]
	ds_read_b128 v[46:49], v25 offset:22528
	ds_read_b128 v[50:53], v25 offset:55296
	v_pk_fma_f32 v[0:1], v[12:13], v[36:37], v[0:1] op_sel_hi:[1,0,1]
	v_fmac_f32_e32 v40, v54, v54
	v_pk_fma_f32 v[0:1], v[14:15], v[38:39], v[0:1] op_sel_hi:[1,0,1]
	s_waitcnt lgkmcnt(1)
	v_fmac_f32_e32 v39, v48, v58
	v_pk_fma_f32 v[0:1], v[42:43], v[54:55], v[0:1] op_sel_hi:[1,0,1]
	v_fmac_f32_e32 v37, v49, v58
	v_pk_fma_f32 v[0:1], v[44:45], v[56:57], v[0:1] op_sel_hi:[1,0,1]
	s_waitcnt lgkmcnt(0)
	v_fmac_f32_e32 v35, v50, v58
	v_pk_fma_f32 v[12:13], v[46:47], v[58:59], v[0:1] op_sel_hi:[1,0,1]
	ds_read_b128 v[0:3], v25 offset:30720
	ds_read_b128 v[4:7], v25 offset:63488
	v_fmac_f32_e32 v33, v51, v58
	v_fmac_f32_e32 v31, v52, v58
	v_fmac_f32_e32 v29, v53, v58
	s_waitcnt lgkmcnt(1)
	v_fmac_f32_e32 v39, v2, v16
	v_fmac_f32_e32 v37, v3, v16
	global_load_dwordx2 v[2:3], v[20:21], off offset:3584
	s_waitcnt lgkmcnt(0)
	v_fmac_f32_e32 v35, v4, v16
	v_fmac_f32_e32 v33, v5, v16
	v_fmac_f32_e32 v31, v6, v16
	v_fmac_f32_e32 v29, v7, v16
	v_fmac_f32_e32 v40, v56, v56
	v_fmac_f32_e32 v40, v58, v58
	v_fmac_f32_e32 v40, v16, v16
	s_waitcnt vmcnt(0)
	v_lshlrev_b32_e32 v24, 16, v2
	v_and_b32_e32 v22, 0xffff0000, v2
	v_lshlrev_b32_e32 v20, 16, v3
	v_and_b32_e32 v14, 0xffff0000, v3
	ds_read_b128 v[2:5], v25 offset:7168
	ds_read_b128 v[6:9], v25 offset:39936
	v_fmac_f32_e32 v40, v24, v24
	v_fmac_f32_e32 v40, v22, v22
	v_fmac_f32_e32 v40, v20, v20
	s_waitcnt lgkmcnt(1)
	v_fmac_f32_e32 v39, v4, v24
	v_fmac_f32_e32 v37, v5, v24
	s_waitcnt lgkmcnt(0)
	v_fmac_f32_e32 v35, v6, v24
	v_fmac_f32_e32 v33, v7, v24
	v_fmac_f32_e32 v31, v8, v24
	v_fmac_f32_e32 v29, v9, v24
	ds_read_b128 v[4:7], v25 offset:15360
	ds_read_b128 v[8:11], v25 offset:48128
	v_fmac_f32_e32 v40, v14, v14
	s_waitcnt lgkmcnt(1)
	v_fmac_f32_e32 v39, v6, v22
	v_fmac_f32_e32 v37, v7, v22
	s_waitcnt lgkmcnt(0)
	v_fmac_f32_e32 v35, v8, v22
	v_fmac_f32_e32 v33, v9, v22
	ds_read_b128 v[6:9], v25 offset:23552
	ds_read_b128 v[42:45], v25 offset:56320
	v_fmac_f32_e32 v31, v10, v22
	v_fmac_f32_e32 v29, v11, v22
	s_waitcnt lgkmcnt(1)
	v_fmac_f32_e32 v39, v8, v20
	v_fmac_f32_e32 v37, v9, v20
	s_waitcnt lgkmcnt(0)
	v_fmac_f32_e32 v35, v42, v20
	v_fmac_f32_e32 v33, v43, v20
	v_fmac_f32_e32 v31, v44, v20
	v_fmac_f32_e32 v29, v45, v20
	ds_read_b128 v[8:11], v25 offset:31744
	ds_read_b128 v[42:45], v25 offset:64512
	s_waitcnt lgkmcnt(1)
	v_fmac_f32_e32 v39, v10, v14
	v_mbcnt_lo_u32_b32 v10, -1, 0
	v_mbcnt_hi_u32_b32 v10, -1, v10
	v_fmac_f32_e32 v37, v11, v14
	v_lshlrev_b32_e32 v10, 2, v10
	v_xor_b32_e32 v10, 4, v10
	ds_bpermute_b32 v10, v10, v40
	v_mbcnt_lo_u32_b32 v11, -1, 0
	v_mbcnt_hi_u32_b32 v11, -1, v11
	s_waitcnt lgkmcnt(1)
	v_fmac_f32_e32 v35, v42, v14
	v_lshlrev_b32_e32 v11, 2, v11
	v_xor_b32_e32 v11, 8, v11
	s_waitcnt lgkmcnt(0)
	v_add_f32_e32 v10, v40, v10
	ds_bpermute_b32 v11, v11, v10
	v_fmac_f32_e32 v33, v43, v14
	v_fmac_f32_e32 v31, v44, v14
	v_fmac_f32_e32 v29, v45, v14
	s_waitcnt lgkmcnt(0)
	v_add_f32_e32 v10, v10, v11
	v_mbcnt_lo_u32_b32 v11, -1, 0
	v_mbcnt_hi_u32_b32 v11, -1, v11
	s_nop 0
	v_lshlrev_b32_e32 v11, 2, v11
	v_xor_b32_e32 v11, 16, v11
	ds_bpermute_b32 v11, v11, v10
	s_waitcnt lgkmcnt(0)
	v_add_f32_e32 v10, v10, v11
	v_mbcnt_lo_u32_b32 v11, -1, 0
	v_mbcnt_hi_u32_b32 v11, -1, v11
	s_nop 0
	v_lshlrev_b32_e32 v11, 2, v11
	v_xor_b32_e32 v11, 32, v11
	ds_bpermute_b32 v11, v11, v10
	s_waitcnt lgkmcnt(0)
	v_add_f32_e32 v10, v10, v11
	v_mbcnt_lo_u32_b32 v11, -1, 0
	v_mbcnt_hi_u32_b32 v11, -1, v11
	s_nop 0
	v_lshlrev_b32_e32 v11, 2, v11
	v_xor_b32_e32 v11, 64, v11
	ds_bpermute_b32 v11, v11, v10
	s_waitcnt lgkmcnt(0)
	v_add_f32_e32 v10, v10, v11
	v_mbcnt_lo_u32_b32 v11, -1, 0
	v_mbcnt_hi_u32_b32 v11, -1, v11
	v_mbcnt_lo_u32_b32 v15, -1, 0
	v_mbcnt_hi_u32_b32 v15, -1, v15
	v_mbcnt_lo_u32_b32 v17, -1, 0
	v_mbcnt_hi_u32_b32 v17, -1, v17
	v_mbcnt_lo_u32_b32 v21, -1, 0
	v_mbcnt_hi_u32_b32 v21, -1, v21
	v_mbcnt_lo_u32_b32 v23, -1, 0
	v_mbcnt_hi_u32_b32 v23, -1, v23
	v_mbcnt_lo_u32_b32 v26, -1, 0
	v_mbcnt_hi_u32_b32 v26, -1, v26
	v_mbcnt_lo_u32_b32 v27, -1, 0
	v_mbcnt_hi_u32_b32 v27, -1, v27
	s_nop 0
	v_lshlrev_b32_e32 v15, 2, v15
	v_lshlrev_b32_e32 v17, 2, v17
	v_xor_b32_e32 v17, 8, v17
	v_lshlrev_b32_e32 v23, 2, v23
	v_pk_fma_f32 v[0:1], v[0:1], v[16:17], v[12:13] op_sel_hi:[1,0,1]
	v_lshlrev_b32_e32 v21, 2, v21
	v_xor_b32_e32 v23, 32, v23
	v_pk_fma_f32 v[0:1], v[2:3], v[24:25], v[0:1] op_sel_hi:[1,0,1]
	v_xor_b32_e32 v21, 16, v21
	v_mbcnt_lo_u32_b32 v28, -1, 0
	v_mbcnt_hi_u32_b32 v28, -1, v28
	v_pk_fma_f32 v[0:1], v[4:5], v[22:23], v[0:1] op_sel_hi:[1,0,1]
	v_xor_b32_e32 v15, 4, v15
	v_lshlrev_b32_e32 v28, 2, v28
	v_pk_fma_f32 v[0:1], v[6:7], v[20:21], v[0:1] op_sel_hi:[1,0,1]
	v_xor_b32_e32 v28, 4, v28
	v_pk_fma_f32 v[0:1], v[8:9], v[14:15], v[0:1] op_sel_hi:[1,0,1]
	ds_bpermute_b32 v2, v15, v0
	ds_bpermute_b32 v3, v28, v1
	v_mbcnt_lo_u32_b32 v30, -1, 0
	v_mbcnt_hi_u32_b32 v30, -1, v30
	v_mbcnt_lo_u32_b32 v32, -1, 0
	v_mbcnt_hi_u32_b32 v32, -1, v32
	v_mbcnt_lo_u32_b32 v34, -1, 0
	v_mbcnt_hi_u32_b32 v34, -1, v34
	v_mbcnt_lo_u32_b32 v36, -1, 0
	v_mbcnt_hi_u32_b32 v36, -1, v36
	s_waitcnt lgkmcnt(0)
	v_pk_add_f32 v[0:1], v[0:1], v[2:3]
	v_lshlrev_b32_e32 v30, 2, v30
	v_xor_b32_e32 v30, 8, v30
	ds_bpermute_b32 v2, v17, v0
	ds_bpermute_b32 v3, v30, v1
	v_lshlrev_b32_e32 v32, 2, v32
	v_xor_b32_e32 v32, 16, v32
	v_lshlrev_b32_e32 v34, 2, v34
	v_xor_b32_e32 v34, 32, v34
	s_waitcnt lgkmcnt(0)
	v_pk_add_f32 v[0:1], v[0:1], v[2:3]
	ds_bpermute_b32 v2, v21, v0
	ds_bpermute_b32 v3, v32, v1
	v_lshlrev_b32_e32 v26, 2, v26
	v_lshlrev_b32_e32 v36, 2, v36
	v_xor_b32_e32 v26, 64, v26
	v_xor_b32_e32 v36, 64, v36
	s_waitcnt lgkmcnt(0)
	v_pk_add_f32 v[0:1], v[0:1], v[2:3]
	ds_bpermute_b32 v2, v23, v0
	ds_bpermute_b32 v3, v34, v1
	v_lshlrev_b32_e32 v11, 2, v11
	v_lshlrev_b32_e32 v27, 2, v27
	v_xor_b32_e32 v11, 0x80, v11
	v_xor_b32_e32 v27, 0x80, v27
	s_waitcnt lgkmcnt(0)
	v_pk_add_f32 v[0:1], v[0:1], v[2:3]
	ds_bpermute_b32 v2, v26, v0
	ds_bpermute_b32 v3, v36, v1
	ds_bpermute_b32 v11, v11, v10
	s_waitcnt lgkmcnt(1)
	v_pk_add_f32 v[0:1], v[0:1], v[2:3]
	v_mbcnt_lo_u32_b32 v3, -1, 0
	v_mbcnt_hi_u32_b32 v3, -1, v3
	v_mbcnt_lo_u32_b32 v4, -1, 0
	v_mbcnt_hi_u32_b32 v4, -1, v4
	v_mbcnt_lo_u32_b32 v5, -1, 0
	v_mbcnt_hi_u32_b32 v5, -1, v5
	ds_bpermute_b32 v2, v27, v0
	v_lshlrev_b32_e32 v4, 2, v4
	v_xor_b32_e32 v4, 4, v4
	ds_bpermute_b32 v4, v4, v39
	v_lshlrev_b32_e32 v5, 2, v5
	v_xor_b32_e32 v5, 8, v5
	v_lshlrev_b32_e32 v3, 2, v3
	v_xor_b32_e32 v3, 0x80, v3
	s_waitcnt lgkmcnt(0)
	v_add_f32_e32 v4, v39, v4
	ds_bpermute_b32 v5, v5, v4
	ds_bpermute_b32 v3, v3, v1
	s_waitcnt lgkmcnt(1)
	v_add_f32_e32 v4, v4, v5
	v_mbcnt_lo_u32_b32 v5, -1, 0
	v_mbcnt_hi_u32_b32 v5, -1, v5
	s_nop 0
	v_lshlrev_b32_e32 v5, 2, v5
	v_xor_b32_e32 v5, 16, v5
	ds_bpermute_b32 v5, v5, v4
	s_waitcnt lgkmcnt(0)
	v_add_f32_e32 v4, v4, v5
	v_mbcnt_lo_u32_b32 v5, -1, 0
	v_mbcnt_hi_u32_b32 v5, -1, v5
	s_nop 0
	v_lshlrev_b32_e32 v5, 2, v5
	v_xor_b32_e32 v5, 32, v5
	ds_bpermute_b32 v5, v5, v4
	s_waitcnt lgkmcnt(0)
	v_add_f32_e32 v4, v4, v5
	v_mbcnt_lo_u32_b32 v5, -1, 0
	v_mbcnt_hi_u32_b32 v5, -1, v5
	s_nop 0
	v_lshlrev_b32_e32 v5, 2, v5
	v_xor_b32_e32 v5, 64, v5
	ds_bpermute_b32 v5, v5, v4
	s_waitcnt lgkmcnt(0)
	v_add_f32_e32 v5, v4, v5
	v_mbcnt_lo_u32_b32 v4, -1, 0
	v_mbcnt_hi_u32_b32 v4, -1, v4
	s_nop 0
	v_lshlrev_b32_e32 v4, 2, v4
	v_xor_b32_e32 v4, 0x80, v4
	ds_bpermute_b32 v6, v4, v5
	v_mbcnt_lo_u32_b32 v4, -1, 0
	v_mbcnt_hi_u32_b32 v4, -1, v4
	v_mbcnt_lo_u32_b32 v7, -1, 0
	v_mbcnt_hi_u32_b32 v7, -1, v7
	s_nop 0
	v_lshlrev_b32_e32 v4, 2, v4
	v_xor_b32_e32 v4, 4, v4
	ds_bpermute_b32 v4, v4, v37
	v_lshlrev_b32_e32 v7, 2, v7
	v_xor_b32_e32 v7, 8, v7
	s_waitcnt lgkmcnt(0)
	v_add_f32_e32 v4, v37, v4
	ds_bpermute_b32 v7, v7, v4
	s_waitcnt lgkmcnt(0)
	v_add_f32_e32 v4, v4, v7
	v_mbcnt_lo_u32_b32 v7, -1, 0
	v_mbcnt_hi_u32_b32 v7, -1, v7
	s_nop 0
	v_lshlrev_b32_e32 v7, 2, v7
	v_xor_b32_e32 v7, 16, v7
	ds_bpermute_b32 v7, v7, v4
	s_waitcnt lgkmcnt(0)
	v_add_f32_e32 v4, v4, v7
	v_mbcnt_lo_u32_b32 v7, -1, 0
	v_mbcnt_hi_u32_b32 v7, -1, v7
	s_nop 0
	v_lshlrev_b32_e32 v7, 2, v7
	v_xor_b32_e32 v7, 32, v7
	ds_bpermute_b32 v7, v7, v4
	s_waitcnt lgkmcnt(0)
	v_add_f32_e32 v4, v4, v7
	v_mbcnt_lo_u32_b32 v7, -1, 0
	v_mbcnt_hi_u32_b32 v7, -1, v7
	s_nop 0
	v_lshlrev_b32_e32 v7, 2, v7
	v_xor_b32_e32 v7, 64, v7
	ds_bpermute_b32 v7, v7, v4
	s_waitcnt lgkmcnt(0)
	v_add_f32_e32 v7, v4, v7
	v_mbcnt_lo_u32_b32 v4, -1, 0
	v_mbcnt_hi_u32_b32 v4, -1, v4
	s_nop 0
	v_lshlrev_b32_e32 v4, 2, v4
	v_xor_b32_e32 v4, 0x80, v4
	ds_bpermute_b32 v8, v4, v7
	v_mbcnt_lo_u32_b32 v4, -1, 0
	v_mbcnt_hi_u32_b32 v4, -1, v4
	v_mbcnt_lo_u32_b32 v9, -1, 0
	v_mbcnt_hi_u32_b32 v9, -1, v9
	s_nop 0
	v_lshlrev_b32_e32 v4, 2, v4
	v_xor_b32_e32 v4, 4, v4
	ds_bpermute_b32 v4, v4, v35
	v_lshlrev_b32_e32 v9, 2, v9
	v_xor_b32_e32 v9, 8, v9
	s_waitcnt lgkmcnt(0)
	v_add_f32_e32 v4, v35, v4
	ds_bpermute_b32 v9, v9, v4
	s_waitcnt lgkmcnt(0)
	v_add_f32_e32 v4, v4, v9
	v_mbcnt_lo_u32_b32 v9, -1, 0
	v_mbcnt_hi_u32_b32 v9, -1, v9
	s_nop 0
	v_lshlrev_b32_e32 v9, 2, v9
	v_xor_b32_e32 v9, 16, v9
	ds_bpermute_b32 v9, v9, v4
	s_waitcnt lgkmcnt(0)
	v_add_f32_e32 v4, v4, v9
	v_mbcnt_lo_u32_b32 v9, -1, 0
	v_mbcnt_hi_u32_b32 v9, -1, v9
	s_nop 0
	v_lshlrev_b32_e32 v9, 2, v9
	v_xor_b32_e32 v9, 32, v9
	ds_bpermute_b32 v9, v9, v4
	s_waitcnt lgkmcnt(0)
	v_add_f32_e32 v4, v4, v9
	v_mbcnt_lo_u32_b32 v9, -1, 0
	v_mbcnt_hi_u32_b32 v9, -1, v9
	s_nop 0
	v_lshlrev_b32_e32 v9, 2, v9
	v_xor_b32_e32 v9, 64, v9
	ds_bpermute_b32 v9, v9, v4
	s_waitcnt lgkmcnt(0)
	v_add_f32_e32 v9, v4, v9
	v_mbcnt_lo_u32_b32 v4, -1, 0
	v_mbcnt_hi_u32_b32 v4, -1, v4
	s_nop 0
	v_lshlrev_b32_e32 v4, 2, v4
	v_xor_b32_e32 v4, 0x80, v4
	ds_bpermute_b32 v12, v4, v9
	v_mbcnt_lo_u32_b32 v4, -1, 0
	v_mbcnt_hi_u32_b32 v4, -1, v4
	v_mbcnt_lo_u32_b32 v13, -1, 0
	v_mbcnt_hi_u32_b32 v13, -1, v13
	s_nop 0
	v_lshlrev_b32_e32 v4, 2, v4
	v_xor_b32_e32 v4, 4, v4
	ds_bpermute_b32 v4, v4, v33
	v_lshlrev_b32_e32 v13, 2, v13
	v_xor_b32_e32 v13, 8, v13
	s_waitcnt lgkmcnt(0)
	v_add_f32_e32 v4, v33, v4
	ds_bpermute_b32 v13, v13, v4
	s_waitcnt lgkmcnt(0)
	v_add_f32_e32 v4, v4, v13
	v_mbcnt_lo_u32_b32 v13, -1, 0
	v_mbcnt_hi_u32_b32 v13, -1, v13
	s_nop 0
	v_lshlrev_b32_e32 v13, 2, v13
	v_xor_b32_e32 v13, 16, v13
	ds_bpermute_b32 v13, v13, v4
	s_waitcnt lgkmcnt(0)
	v_add_f32_e32 v4, v4, v13
	v_mbcnt_lo_u32_b32 v13, -1, 0
	v_mbcnt_hi_u32_b32 v13, -1, v13
	s_nop 0
	v_lshlrev_b32_e32 v13, 2, v13
	v_xor_b32_e32 v13, 32, v13
	ds_bpermute_b32 v13, v13, v4
	s_waitcnt lgkmcnt(0)
	v_add_f32_e32 v4, v4, v13
	v_mbcnt_lo_u32_b32 v13, -1, 0
	v_mbcnt_hi_u32_b32 v13, -1, v13
	s_nop 0
	v_lshlrev_b32_e32 v13, 2, v13
	v_xor_b32_e32 v13, 64, v13
	ds_bpermute_b32 v13, v13, v4
	s_waitcnt lgkmcnt(0)
	v_add_f32_e32 v13, v4, v13
	v_mbcnt_lo_u32_b32 v4, -1, 0
	v_mbcnt_hi_u32_b32 v4, -1, v4
	s_nop 0
	v_lshlrev_b32_e32 v4, 2, v4
	v_xor_b32_e32 v4, 0x80, v4
	ds_bpermute_b32 v14, v4, v13
	v_mbcnt_lo_u32_b32 v4, -1, 0
	v_mbcnt_hi_u32_b32 v4, -1, v4
	v_mbcnt_lo_u32_b32 v15, -1, 0
	v_mbcnt_hi_u32_b32 v15, -1, v15
	s_nop 0
	v_lshlrev_b32_e32 v4, 2, v4
	v_xor_b32_e32 v4, 4, v4
	ds_bpermute_b32 v4, v4, v31
	v_lshlrev_b32_e32 v15, 2, v15
	v_xor_b32_e32 v15, 8, v15
	s_waitcnt lgkmcnt(0)
	v_add_f32_e32 v4, v31, v4
	ds_bpermute_b32 v15, v15, v4
	s_waitcnt lgkmcnt(0)
	v_add_f32_e32 v4, v4, v15
	v_mbcnt_lo_u32_b32 v15, -1, 0
	v_mbcnt_hi_u32_b32 v15, -1, v15
	s_nop 0
	v_lshlrev_b32_e32 v15, 2, v15
	v_xor_b32_e32 v15, 16, v15
	ds_bpermute_b32 v15, v15, v4
	s_waitcnt lgkmcnt(0)
	v_add_f32_e32 v4, v4, v15
	v_mbcnt_lo_u32_b32 v15, -1, 0
	v_mbcnt_hi_u32_b32 v15, -1, v15
	s_nop 0
	v_lshlrev_b32_e32 v15, 2, v15
	v_xor_b32_e32 v15, 32, v15
	ds_bpermute_b32 v15, v15, v4
	s_waitcnt lgkmcnt(0)
	v_add_f32_e32 v4, v4, v15
	v_mbcnt_lo_u32_b32 v15, -1, 0
	v_mbcnt_hi_u32_b32 v15, -1, v15
	s_nop 0
	v_lshlrev_b32_e32 v15, 2, v15
	v_xor_b32_e32 v15, 64, v15
	ds_bpermute_b32 v15, v15, v4
	s_waitcnt lgkmcnt(0)
	v_add_f32_e32 v15, v4, v15
	v_mbcnt_lo_u32_b32 v4, -1, 0
	v_mbcnt_hi_u32_b32 v4, -1, v4
	s_nop 0
	v_lshlrev_b32_e32 v4, 2, v4
	v_xor_b32_e32 v4, 0x80, v4
	ds_bpermute_b32 v16, v4, v15
	v_mbcnt_lo_u32_b32 v4, -1, 0
	v_mbcnt_hi_u32_b32 v4, -1, v4
	v_mbcnt_lo_u32_b32 v17, -1, 0
	v_mbcnt_hi_u32_b32 v17, -1, v17
	s_nop 0
	v_lshlrev_b32_e32 v4, 2, v4
	v_xor_b32_e32 v4, 4, v4
	ds_bpermute_b32 v4, v4, v29
	v_lshlrev_b32_e32 v17, 2, v17
	v_xor_b32_e32 v17, 8, v17
	s_waitcnt lgkmcnt(0)
	v_add_f32_e32 v4, v29, v4
	ds_bpermute_b32 v17, v17, v4
	s_waitcnt lgkmcnt(0)
	v_add_f32_e32 v4, v4, v17
	v_mbcnt_lo_u32_b32 v17, -1, 0
	v_mbcnt_hi_u32_b32 v17, -1, v17
	s_nop 0
	v_lshlrev_b32_e32 v17, 2, v17
	v_xor_b32_e32 v17, 16, v17
	ds_bpermute_b32 v17, v17, v4
	s_waitcnt lgkmcnt(0)
	v_add_f32_e32 v4, v4, v17
	v_mbcnt_lo_u32_b32 v17, -1, 0
	v_mbcnt_hi_u32_b32 v17, -1, v17
	s_nop 0
	v_lshlrev_b32_e32 v17, 2, v17
	v_xor_b32_e32 v17, 32, v17
	ds_bpermute_b32 v17, v17, v4
	s_waitcnt lgkmcnt(0)
	v_add_f32_e32 v4, v4, v17
	v_mbcnt_lo_u32_b32 v17, -1, 0
	v_mbcnt_hi_u32_b32 v17, -1, v17
	s_nop 0
	v_lshlrev_b32_e32 v17, 2, v17
	v_xor_b32_e32 v17, 64, v17
	ds_bpermute_b32 v17, v17, v4
	s_waitcnt lgkmcnt(0)
	v_add_f32_e32 v17, v4, v17
	v_mbcnt_lo_u32_b32 v4, -1, 0
	v_mbcnt_hi_u32_b32 v4, -1, v4
	s_nop 0
	v_lshlrev_b32_e32 v4, 2, v4
	v_xor_b32_e32 v4, 0x80, v4
	ds_bpermute_b32 v20, v4, v17
	s_and_saveexec_b64 s[0:1], s[36:37]
	s_cbranch_execz .LBB0_1621
	v_add_f32_e32 v4, v10, v11
	v_fmamk_f32 v4, v4, 0x3a000000, v253
	s_mov_b32 s13, 0xf800000
	v_cmp_gt_f32_e32 vcc, s13, v4
	v_mul_f32_e32 v10, 0x4f800000, v4
	v_add_f32_e32 v5, v5, v6
	v_cndmask_b32_e32 v4, v4, v10, vcc
	v_sqrt_f32_e32 v10, v4
	v_pk_add_f32 v[0:1], v[0:1], v[2:3]
	v_add_f32_e32 v7, v7, v8
	v_add_f32_e32 v9, v9, v12
	v_add_u32_e32 v11, -1, v10
	v_fma_f32 v21, -v11, v10, v4
	v_cmp_ge_f32_e64 s[38:39], 0, v21
	v_add_u32_e32 v21, 1, v10
	v_add_f32_e32 v13, v13, v14
	v_cndmask_b32_e64 v11, v10, v11, s[38:39]
	v_fma_f32 v10, -v21, v10, v4
	v_cmp_lt_f32_e64 s[38:39], 0, v10
	s_nop 1
	v_cndmask_b32_e64 v10, v11, v21, s[38:39]
	v_mul_f32_e32 v11, 0x37800000, v10
	v_cndmask_b32_e32 v10, v10, v11, vcc
	v_mov_b32_e32 v11, 0x260
	v_cmp_class_f32_e32 vcc, v4, v11
	s_nop 1
	v_cndmask_b32_e32 v4, v10, v4, vcc
	v_div_scale_f32 v10, s[18:19], v4, v4, 1.0
	v_rcp_f32_e32 v11, v10
	s_nop 0
	v_fma_f32 v21, -v10, v11, 1.0
	v_fmac_f32_e32 v11, v21, v11
	v_div_scale_f32 v21, vcc, 1.0, v4, 1.0
	v_mul_f32_e32 v22, v21, v11
	v_fma_f32 v23, -v10, v22, v21
	v_fmac_f32_e32 v22, v23, v11
	v_fma_f32 v10, -v10, v22, v21
	v_div_fmas_f32 v10, v10, v11, v22
	v_div_fixup_f32 v4, v10, v4, 1.0
	v_mul_f32_e32 v5, v4, v5
	v_pk_mul_f32 v[0:1], v[4:5], v[0:1] op_sel_hi:[0,1]
	v_cmp_gt_f32_e32 vcc, v1, v0
	v_mul_f32_e32 v7, v4, v7
	v_mul_f32_e32 v9, v4, v9
	v_cndmask_b32_e32 v2, v0, v1, vcc
	v_cmp_gt_f32_e64 s[38:39], v5, v2
	v_mul_f32_e32 v13, v4, v13
	v_cndmask_b32_e64 v3, 0, 1, vcc
	v_cndmask_b32_e64 v2, v2, v5, s[38:39]
	v_cmp_gt_f32_e64 s[40:41], v7, v2
	v_add_f32_e32 v11, v15, v16
	v_cndmask_b32_e64 v3, v3, 2, s[38:39]
	v_cndmask_b32_e64 v2, v2, v7, s[40:41]
	v_cmp_gt_f32_e64 s[42:43], v9, v2
	v_mul_f32_e32 v11, v4, v11
	v_cndmask_b32_e64 v3, v3, 3, s[40:41]
	v_cndmask_b32_e64 v2, v2, v9, s[42:43]
	v_cmp_gt_f32_e64 s[44:45], v13, v2
	s_waitcnt lgkmcnt(0)
	v_add_f32_e32 v10, v17, v20
	v_cndmask_b32_e64 v3, v3, 4, s[42:43]
	v_cndmask_b32_e64 v2, v2, v13, s[44:45]
	v_cmp_gt_f32_e64 s[46:47], v11, v2
	v_mul_f32_e32 v10, v4, v10
	v_cndmask_b32_e64 v3, v3, 5, s[44:45]
	v_cndmask_b32_e64 v2, v2, v11, s[46:47]
	v_cmp_ngt_f32_e64 s[48:49], v10, v2
	v_cndmask_b32_e64 v3, v3, 6, s[46:47]
	s_and_b64 s[18:19], s[48:49], s[46:47]
	v_cndmask_b32_e64 v176, 7, v3, s[48:49]
	v_cmp_ne_u32_e64 s[46:47], 0, v176
	v_cmp_lt_f32_e64 s[50:51], s11, v0
	s_and_b64 s[46:47], s[46:47], s[50:51]
	v_mov_b32_e32 v3, 0xff61b1e6
	v_cndmask_b32_e64 v0, v3, v0, s[46:47]
	v_cmp_ne_u32_e64 s[44:45], 1, v176
	v_cmp_gt_f32_e64 s[46:47], v1, v0
	s_and_b64 s[44:45], s[44:45], s[46:47]
	v_cndmask_b32_e64 v0, v0, v1, s[44:45]
	v_cmp_ne_u32_e64 s[42:43], 2, v176
	v_cmp_gt_f32_e64 s[46:47], v5, v0
	s_and_b64 s[42:43], s[42:43], s[46:47]
	v_cndmask_b32_e64 v0, v0, v5, s[42:43]
	v_cmp_ne_u32_e64 s[40:41], 3, v176
	v_cmp_gt_f32_e64 s[46:47], v7, v0
	s_and_b64 s[40:41], s[40:41], s[46:47]
	v_cndmask_b32_e64 v0, v0, v7, s[40:41]
	v_cmp_ne_u32_e64 s[38:39], 4, v176
	v_cmp_gt_f32_e64 s[46:47], v9, v0
	s_and_b64 s[38:39], s[38:39], s[46:47]
	v_cndmask_b32_e64 v0, v0, v9, s[38:39]
	v_cmp_ne_u32_e32 vcc, 5, v176
	v_cmp_gt_f32_e64 s[46:47], v13, v0
	s_and_b64 vcc, vcc, s[46:47]
	v_cndmask_b32_e32 v0, v0, v13, vcc
	v_cmp_ngt_f32_e64 s[46:47], v11, v0
	s_or_b64 s[46:47], s[18:19], s[46:47]
	v_cndmask_b32_e64 v2, v10, v2, s[48:49]
	v_cndmask_b32_e64 v1, v11, v0, s[46:47]
	v_cmp_gt_f32_e64 s[50:51], v10, v1
	s_and_b64 s[50:51], s[48:49], s[50:51]
	v_cndmask_b32_e64 v0, 0, 1, s[44:45]
	v_cndmask_b32_e64 v1, v1, v10, s[50:51]
	v_sub_f32_e32 v1, v2, v1
	v_mul_f32_e32 v1, 0x3fb8aa3b, v1
	v_exp_f32_e32 v1, v1
	v_cndmask_b32_e64 v0, v0, 2, s[42:43]
	v_cndmask_b32_e64 v0, v0, 3, s[40:41]
	v_cndmask_b32_e64 v0, v0, 4, s[38:39]
	v_add_f32_e32 v1, 1.0, v1
	v_div_scale_f32 v2, s[18:19], v1, v1, 1.0
	v_rcp_f32_e32 v3, v2
	v_cndmask_b32_e64 v0, v0, 5, vcc
	s_add_u32 s18, s52, s8
	s_addc_u32 s19, s53, s9
	v_fma_f32 v5, -v2, v3, 1.0
	v_fmac_f32_e32 v3, v5, v3
	v_div_scale_f32 v5, vcc, 1.0, v1, 1.0
	v_mul_f32_e32 v6, v5, v3
	v_fma_f32 v7, -v2, v6, v5
	v_fmac_f32_e32 v6, v7, v3
	v_fma_f32 v2, -v2, v6, v5
	v_div_fmas_f32 v2, v2, v3, v6
	v_div_fixup_f32 v5, v2, v1, 1.0
	global_store_dword v177, v4, s[18:19]
	v_mul_u32_u24_e32 v2, 0x2100, v176
	v_mov_b32_e32 v3, v177
	v_lshl_add_u64 v[2:3], v[2:3], 0, s[52:53]
	global_atomic_add v1, v[2:3], v231, off offset:384 sc0
	v_cndmask_b32_e64 v0, 6, v0, s[46:47]
	v_cndmask_b32_e64 v0, v0, 7, s[50:51]
	v_mov_b32_e32 v11, s56
	s_ashr_i32 s67, s66, 31
	s_lshl_b64 s[18:19], s[66:67], 2
	s_add_u32 s20, s2, s18
	s_addc_u32 s21, s3, s19
	s_add_i32 s22, s66, 1
	s_ashr_i32 s23, s22, 31
	s_add_u32 s18, s4, s18
	v_sub_f32_e32 v10, 1.0, v5
	s_addc_u32 s19, s5, s19
	s_waitcnt vmcnt(0)
	v_lshl_add_u32 v176, v176, 14, v1
	v_lshlrev_b64 v[2:3], 2, v[176:177]
	v_lshl_add_u64 v[6:7], s[68:69], 0, v[2:3]
	v_mov_b32_e32 v1, v177
	global_store_dword v[6:7], v11, off
	v_mul_u32_u24_e32 v6, 0x2100, v0
	v_mov_b32_e32 v7, v1
	v_lshl_add_u64 v[6:7], v[6:7], 0, s[52:53]
	global_atomic_add v1, v[6:7], v231, off offset:384 sc0
	v_lshl_add_u64 v[2:3], s[70:71], 0, v[2:3]
	global_store_dword v[2:3], v4, off
	s_waitcnt vmcnt(1)
	v_lshl_add_u32 v0, v0, 14, v1
	v_mov_b32_e32 v1, v177
	v_lshlrev_b64 v[6:7], 2, v[0:1]
	v_lshl_add_u64 v[2:3], s[70:71], 0, v[6:7]
	global_store_dword v[2:3], v4, off
	global_store_dword v177, v10, s[18:19]
	s_lshl_b64 s[18:19], s[22:23], 2
	s_add_u32 s18, s4, s18
	v_lshl_add_u64 v[8:9], s[68:69], 0, v[6:7]
	v_mov_b32_e32 v2, v176
	v_mov_b32_e32 v3, v0
	s_addc_u32 s19, s5, s19
	global_store_dword v[8:9], v11, off
	global_store_dwordx2 v177, v[2:3], s[20:21]
	global_store_dword v177, v5, s[18:19]
	s_branch .LBB0_1621

.LBB0_1674:
	s_andn2_b64 vcc, exec, s[0:1]
	s_cbranch_vccnz .LBB0_1790
	v_mbcnt_lo_u32_b32 v0, -1, 0
	v_mbcnt_hi_u32_b32 v0, -1, v0
	v_readlane_b32 s0, v254, 2
	v_add_u32_e32 v0, s79, v0
	v_readlane_b32 s1, v254, 3
	s_load_dword s33, s[0:1], 0x0
	s_mov_b32 s61, s96
	s_mov_b32 s0, 24
	s_waitcnt lgkmcnt(0)
	s_ashr_i32 s1, s0, 31
	s_lshl_b64 s[0:1], s[0:1], 3
	s_add_u32 s0, s92, s0
	s_addc_u32 s1, s93, s1
	s_load_dwordx2 s[18:19], s[0:1], 0x0
	s_movk_i32 s0, 0xa0
	v_cmp_gt_i32_e32 vcc, s0, v0
	s_and_saveexec_b64 s[0:1], vcc
	s_cbranch_execz .LBB0_1694
	s_waitcnt lgkmcnt(0)
	global_load_dword v1, v177, s[18:19] offset:384
	v_cmp_eq_u32_e32 vcc, 0, v0
	s_and_saveexec_b64 s[2:3], vcc
	s_cbranch_execz .LBB0_1678
	v_readlane_b32 s4, v254, 57
	s_nop 1
	v_mov_b32_e32 v2, s4
	v_readlane_b32 s4, v254, 58
	s_waitcnt vmcnt(0)
	ds_write_b32 v2, v1
	v_mov_b32_e32 v2, s4
	ds_write_b32 v2, v177
.LBB0_1678:
	s_or_b64 exec, exec, s[2:3]
	v_mov_b32_e32 v2, 0x2100
	global_load_dword v2, v2, s[18:19] offset:384
	s_waitcnt vmcnt(1)
	v_add_u32_e32 v1, 0xff, v1
	v_ashrrev_i32_e32 v1, 8, v1
	v_cmp_eq_u32_e32 vcc, 1, v0
	s_and_saveexec_b64 s[2:3], vcc
	s_cbranch_execz .LBB0_1680
	v_readlane_b32 s4, v254, 59
	s_nop 1
	v_mov_b32_e32 v3, s4
	v_readlane_b32 s4, v254, 60
	s_waitcnt vmcnt(0)
	ds_write_b32 v3, v2
	v_mov_b32_e32 v3, s4
	ds_write_b32 v3, v1
.LBB0_1680:
	s_or_b64 exec, exec, s[2:3]
	v_mov_b32_e32 v3, 0x4200
	global_load_dword v3, v3, s[18:19] offset:384
	s_waitcnt vmcnt(1)
	v_add_u32_e32 v2, 0xff, v2
	v_ashrrev_i32_e32 v2, 8, v2
	v_add_u32_e32 v2, v2, v1
	v_cmp_eq_u32_e32 vcc, 2, v0
	s_and_saveexec_b64 s[2:3], vcc
	s_cbranch_execz .LBB0_1682
	v_readlane_b32 s4, v254, 61
	s_nop 1
	v_mov_b32_e32 v4, s4
	v_readlane_b32 s4, v254, 62
	s_waitcnt vmcnt(0)
	ds_write_b32 v4, v3
	v_mov_b32_e32 v4, s4
	ds_write_b32 v4, v2
.LBB0_1682:
	s_or_b64 exec, exec, s[2:3]
	v_mov_b32_e32 v4, 0x6300
	global_load_dword v4, v4, s[18:19] offset:384
	s_waitcnt vmcnt(1)
	v_add_u32_e32 v3, 0xff, v3
	v_ashrrev_i32_e32 v3, 8, v3
	v_add_u32_e32 v3, v3, v2
	v_cmp_eq_u32_e32 vcc, 3, v0
	s_and_saveexec_b64 s[2:3], vcc
	s_cbranch_execz .LBB0_1684
	v_readlane_b32 s4, v254, 63
	s_nop 1
	v_mov_b32_e32 v5, s4
	v_readlane_b32 s4, v255, 0
	s_waitcnt vmcnt(0)
	ds_write_b32 v5, v4
	v_mov_b32_e32 v5, s4
	ds_write_b32 v5, v3
.LBB0_1684:
	s_or_b64 exec, exec, s[2:3]
	v_mov_b32_e32 v5, 0x8400
	global_load_dword v5, v5, s[18:19] offset:384
	s_waitcnt vmcnt(1)
	v_add_u32_e32 v4, 0xff, v4
	v_ashrrev_i32_e32 v4, 8, v4
	v_add_u32_e32 v4, v4, v3
	v_cmp_eq_u32_e32 vcc, 4, v0
	s_and_saveexec_b64 s[2:3], vcc
	s_cbranch_execz .LBB0_1686
	v_readlane_b32 s4, v255, 1
	s_nop 1
	v_mov_b32_e32 v6, s4
	v_readlane_b32 s4, v255, 2
	s_waitcnt vmcnt(0)
	ds_write_b32 v6, v5
	v_mov_b32_e32 v6, s4
	ds_write_b32 v6, v4
.LBB0_1686:
	s_or_b64 exec, exec, s[2:3]
	v_mov_b32_e32 v6, 0xa500
	global_load_dword v6, v6, s[18:19] offset:384
	s_waitcnt vmcnt(1)
	v_add_u32_e32 v5, 0xff, v5
	v_ashrrev_i32_e32 v5, 8, v5
	v_add_u32_e32 v5, v5, v4
	v_cmp_eq_u32_e32 vcc, 5, v0
	s_and_saveexec_b64 s[2:3], vcc
	s_cbranch_execz .LBB0_1688
	v_readlane_b32 s4, v255, 3
	s_nop 1
	v_mov_b32_e32 v7, s4
	v_readlane_b32 s4, v255, 4
	s_waitcnt vmcnt(0)
	ds_write_b32 v7, v6
	v_mov_b32_e32 v7, s4
	ds_write_b32 v7, v5
.LBB0_1688:
	s_or_b64 exec, exec, s[2:3]
	v_mov_b32_e32 v7, 0xc600
	global_load_dword v7, v7, s[18:19] offset:384
	s_waitcnt vmcnt(1)
	v_add_u32_e32 v6, 0xff, v6
	v_ashrrev_i32_e32 v6, 8, v6
	v_add_u32_e32 v6, v6, v5
	v_cmp_eq_u32_e32 vcc, 6, v0
	s_and_saveexec_b64 s[2:3], vcc
	s_cbranch_execz .LBB0_1690
	v_readlane_b32 s4, v255, 5
	s_nop 1
	v_mov_b32_e32 v8, s4
	v_readlane_b32 s4, v255, 6
	s_waitcnt vmcnt(0)
	ds_write_b32 v8, v7
	v_mov_b32_e32 v8, s4
	ds_write_b32 v8, v6
.LBB0_1690:
	s_or_b64 exec, exec, s[2:3]
	v_mov_b32_e32 v8, 0xe700
	global_load_dword v8, v8, s[18:19] offset:384
	s_waitcnt vmcnt(1)
	v_add_u32_e32 v7, 0xff, v7
	v_ashrrev_i32_e32 v7, 8, v7
	v_add_u32_e32 v7, v7, v6
	v_cmp_eq_u32_e32 vcc, 7, v0
	s_and_saveexec_b64 s[2:3], vcc
	s_cbranch_execz .LBB0_1692
	v_readlane_b32 s4, v255, 7
	s_nop 1
	v_mov_b32_e32 v9, s4
	v_readlane_b32 s4, v255, 8
	s_waitcnt vmcnt(0)
	ds_write_b32 v9, v8
	v_mov_b32_e32 v9, s4
	ds_write_b32 v9, v7

.LBB0_1792:
	s_andn2_b64 vcc, exec, s[0:1]
	s_cbranch_vccnz .LBB0_1880
	v_mbcnt_lo_u32_b32 v0, -1, 0
	v_mbcnt_hi_u32_b32 v0, -1, v0
	v_readlane_b32 s0, v254, 2
	v_add_u32_e32 v0, s79, v0
	v_readlane_b32 s1, v254, 3
	s_load_dword s33, s[0:1], 0x0
	s_mov_b32 s34, s96
	s_mov_b32 s0, 24
	s_waitcnt lgkmcnt(0)
	s_ashr_i32 s1, s0, 31
	s_lshl_b64 s[0:1], s[0:1], 3
	s_add_u32 s0, s92, s0
	s_addc_u32 s1, s93, s1
	s_load_dwordx2 s[2:3], s[0:1], 0x0
	s_movk_i32 s0, 0xa0
	v_cmp_gt_i32_e32 vcc, s0, v0
	s_and_saveexec_b64 s[0:1], vcc
	s_cbranch_execz .LBB0_1812
	s_waitcnt lgkmcnt(0)
	global_load_dword v1, v177, s[2:3] offset:384
	v_cmp_eq_u32_e32 vcc, 0, v0
	s_and_saveexec_b64 s[4:5], vcc
	s_cbranch_execz .LBB0_1796
	v_readlane_b32 s8, v254, 57
	s_nop 1
	v_mov_b32_e32 v2, s8
	v_readlane_b32 s8, v254, 58
	s_waitcnt vmcnt(0)
	ds_write_b32 v2, v1
	v_mov_b32_e32 v2, s8
	ds_write_b32 v2, v177
.LBB0_1796:
	s_or_b64 exec, exec, s[4:5]
	v_mov_b32_e32 v2, 0x2100
	global_load_dword v2, v2, s[2:3] offset:384
	s_waitcnt vmcnt(1)
	v_add_u32_e32 v1, 0xff, v1
	v_ashrrev_i32_e32 v1, 8, v1
	v_cmp_eq_u32_e32 vcc, 1, v0
	s_and_saveexec_b64 s[4:5], vcc
	s_cbranch_execz .LBB0_1798
	v_readlane_b32 s8, v254, 59
	s_nop 1
	v_mov_b32_e32 v3, s8
	v_readlane_b32 s8, v254, 60
	s_waitcnt vmcnt(0)
	ds_write_b32 v3, v2
	v_mov_b32_e32 v3, s8
	ds_write_b32 v3, v1
.LBB0_1798:
	s_or_b64 exec, exec, s[4:5]
	v_mov_b32_e32 v3, 0x4200
	global_load_dword v3, v3, s[2:3] offset:384
	s_waitcnt vmcnt(1)
	v_add_u32_e32 v2, 0xff, v2
	v_ashrrev_i32_e32 v2, 8, v2
	v_add_u32_e32 v2, v2, v1
	v_cmp_eq_u32_e32 vcc, 2, v0
	s_and_saveexec_b64 s[4:5], vcc
	s_cbranch_execz .LBB0_1800
	v_readlane_b32 s8, v254, 61
	s_nop 1
	v_mov_b32_e32 v4, s8
	v_readlane_b32 s8, v254, 62
	s_waitcnt vmcnt(0)
	ds_write_b32 v4, v3
	v_mov_b32_e32 v4, s8
	ds_write_b32 v4, v2
.LBB0_1800:
	s_or_b64 exec, exec, s[4:5]
	v_mov_b32_e32 v4, 0x6300
	global_load_dword v4, v4, s[2:3] offset:384
	s_waitcnt vmcnt(1)
	v_add_u32_e32 v3, 0xff, v3
	v_ashrrev_i32_e32 v3, 8, v3
	v_add_u32_e32 v3, v3, v2
	v_cmp_eq_u32_e32 vcc, 3, v0
	s_and_saveexec_b64 s[4:5], vcc
	s_cbranch_execz .LBB0_1802
	v_readlane_b32 s8, v254, 63
	s_nop 1
	v_mov_b32_e32 v5, s8
	v_readlane_b32 s8, v255, 0
	s_waitcnt vmcnt(0)
	ds_write_b32 v5, v4
	v_mov_b32_e32 v5, s8
	ds_write_b32 v5, v3
.LBB0_1802:
	s_or_b64 exec, exec, s[4:5]
	v_mov_b32_e32 v5, 0x8400
	global_load_dword v5, v5, s[2:3] offset:384
	s_waitcnt vmcnt(1)
	v_add_u32_e32 v4, 0xff, v4
	v_ashrrev_i32_e32 v4, 8, v4
	v_add_u32_e32 v4, v4, v3
	v_cmp_eq_u32_e32 vcc, 4, v0
	s_and_saveexec_b64 s[4:5], vcc
	s_cbranch_execz .LBB0_1804
	v_readlane_b32 s8, v255, 1
	s_nop 1
	v_mov_b32_e32 v6, s8
	v_readlane_b32 s8, v255, 2
	s_waitcnt vmcnt(0)
	ds_write_b32 v6, v5
	v_mov_b32_e32 v6, s8
	ds_write_b32 v6, v4
.LBB0_1804:
	s_or_b64 exec, exec, s[4:5]
	v_mov_b32_e32 v6, 0xa500
	global_load_dword v6, v6, s[2:3] offset:384
	s_waitcnt vmcnt(1)
	v_add_u32_e32 v5, 0xff, v5
	v_ashrrev_i32_e32 v5, 8, v5
	v_add_u32_e32 v5, v5, v4
	v_cmp_eq_u32_e32 vcc, 5, v0
	s_and_saveexec_b64 s[4:5], vcc
	s_cbranch_execz .LBB0_1806
	v_readlane_b32 s8, v255, 3
	s_nop 1
	v_mov_b32_e32 v7, s8
	v_readlane_b32 s8, v255, 4
	s_waitcnt vmcnt(0)
	ds_write_b32 v7, v6
	v_mov_b32_e32 v7, s8
	ds_write_b32 v7, v5
.LBB0_1806:
	s_or_b64 exec, exec, s[4:5]
	v_mov_b32_e32 v7, 0xc600
	global_load_dword v7, v7, s[2:3] offset:384
	s_waitcnt vmcnt(1)
	v_add_u32_e32 v6, 0xff, v6
	v_ashrrev_i32_e32 v6, 8, v6
	v_add_u32_e32 v6, v6, v5
	v_cmp_eq_u32_e32 vcc, 6, v0
	s_and_saveexec_b64 s[4:5], vcc
	s_cbranch_execz .LBB0_1808
	v_readlane_b32 s8, v255, 5
	s_nop 1
	v_mov_b32_e32 v8, s8
	v_readlane_b32 s8, v255, 6
	s_waitcnt vmcnt(0)
	ds_write_b32 v8, v7
	v_mov_b32_e32 v8, s8
	ds_write_b32 v8, v6
.LBB0_1808:
	s_or_b64 exec, exec, s[4:5]
	v_mov_b32_e32 v8, 0xe700
	global_load_dword v8, v8, s[2:3] offset:384
	s_waitcnt vmcnt(1)
	v_add_u32_e32 v7, 0xff, v7
	v_ashrrev_i32_e32 v7, 8, v7
	v_add_u32_e32 v7, v7, v6
	v_cmp_eq_u32_e32 vcc, 7, v0
	s_and_saveexec_b64 s[4:5], vcc
	s_cbranch_execz .LBB0_1810
	v_readlane_b32 s8, v255, 7
	s_nop 1
	v_mov_b32_e32 v9, s8
	v_readlane_b32 s8, v255, 8
	s_waitcnt vmcnt(0)
	ds_write_b32 v9, v8
	v_mov_b32_e32 v9, s8
	ds_write_b32 v9, v7

.LBB0_1883:
	s_lshl_b32 s0, s8, 3
	s_add_i32 s0, s0, s91
	s_mov_b32 s4, 24
	s_mov_b32 s2, 23
	s_cmpk_gt_i32 s0, 0x3fff
	s_cbranch_scc1 .LBB0_1886
	s_ashr_i32 s5, s4, 31
	s_lshl_b64 s[4:5], s[4:5], 3
	s_add_u32 s4, s92, s4
	s_addc_u32 s5, s93, s5
	s_load_dwordx2 s[4:5], s[4:5], 0x0
	v_lshlrev_b32_e32 v0, 3, v2
	v_and_b32_e32 v176, 0x1f8, v0
	s_mov_b64 s[34:35], 0x48600000
	s_waitcnt lgkmcnt(0)
	v_mov_b32_e32 v4, 0x8400
	global_load_dword v4, v4, s[4:5] offset:384
	v_mov_b32_e32 v5, 0xa500
	global_load_dword v5, v5, s[4:5] offset:384
	v_mov_b32_e32 v6, 0xc600
	global_load_dword v6, v6, s[4:5] offset:384
	s_add_u32 s18, s4, 0x440000
	s_addc_u32 s19, s5, 0
	s_ashr_i32 s3, s2, 31
	s_lshl_b64 s[2:3], s[2:3], 3
	s_add_u32 s2, s92, s2
	s_addc_u32 s3, s93, s3
	s_load_dwordx2 s[12:13], s[2:3], 0x0
	v_lshl_add_u64 v[0:1], s[4:5], 0, v[176:177]
	v_lshl_add_u64 v[0:1], v[0:1], 0, s[34:35]
	s_waitcnt vmcnt(0)
	v_readfirstlane_b32 s1, v6
	v_readfirstlane_b32 s2, v5
	v_readfirstlane_b32 s3, v4
	global_load_dword v4, v177, s[4:5] offset:384
	v_mov_b32_e32 v5, 0x2100
	global_load_dword v5, v5, s[4:5] offset:384
	v_mov_b32_e32 v6, 0x4200
	global_load_dword v6, v6, s[4:5] offset:384
	v_mov_b32_e32 v7, 0x6300
	global_load_dword v7, v7, s[4:5] offset:384
	s_addk_i32 s3, 0xff
	s_ashr_i32 s28, s3, 8
	s_addk_i32 s2, 0xff
	s_ashr_i32 s29, s2, 8
	s_addk_i32 s1, 0xff
	s_ashr_i32 s30, s1, 8
	s_lshl_b32 s2, s9, 3
	s_waitcnt vmcnt(0)
	v_readfirstlane_b32 s21, v5
	v_readfirstlane_b32 s20, v4
	v_readfirstlane_b32 s22, v6
	s_addk_i32 s20, 0xff
	s_addk_i32 s21, 0xff
	v_readfirstlane_b32 s23, v7
	s_ashr_i32 s20, s20, 8
	s_ashr_i32 s21, s21, 8
	s_addk_i32 s22, 0xff
	s_add_i32 s21, s21, s20
	s_ashr_i32 s22, s22, 8
	s_addk_i32 s23, 0xff
	s_add_i32 s22, s22, s21
	s_ashr_i32 s23, s23, 8
	s_add_i32 s23, s23, s22
	s_add_i32 s28, s28, s23
	s_add_i32 s29, s29, s28
	s_add_i32 s30, s30, s29
	s_add_u32 s31, s4, 0x420000
	s_addc_u32 s33, s5, 0
	s_ashr_i32 s1, s0, 31
	s_lshl_b64 s[34:35], s[0:1], 12
	v_and_b32_e32 v4, 63, v2
	s_add_u32 s4, s4, s34
	v_lshlrev_b32_e32 v176, 3, v4
	s_addc_u32 s5, s5, s35
	v_lshl_add_u64 v[2:3], s[4:5], 0, v[176:177]
	s_mov_b64 s[4:5], 0x2d000000
	s_ashr_i32 s3, s2, 31
	s_lshl_b32 s8, s8, 4
	v_readlane_b32 s34, v254, 53
	v_lshl_add_u64 v[2:3], v[2:3], 0, s[4:5]
	s_lshl_b64 s[4:5], s[2:3], 12
	s_add_i32 s8, s34, s8
	s_lshl_b32 s34, s9, 4
	s_lshl_b64 s[36:37], s[0:1], 13
	s_waitcnt lgkmcnt(0)
	s_add_u32 s12, s12, s36
	v_lshlrev_b32_e32 v176, 4, v4
	s_addc_u32 s13, s13, s37
	v_lshl_add_u64 v[4:5], s[12:13], 0, v[176:177]
	s_mov_b64 s[12:13], 0x1000
	v_lshl_add_u64 v[4:5], v[4:5], 0, s[12:13]
	s_lshl_b64 s[12:13], s[2:3], 13
